# P7: per-step fp8 store issued after the next step's three parameter loads (data kept in a free register), waits leave the store in flight
# baseline (speedup 1.0000x reference)
.LBB0_682:
	v_lshl_add_u64 v[2:3], s[76:77], 0, v[28:29]
	v_add_co_u32_e32 v30, vcc, 0x54768000, v2
	s_add_i32 s22, s14, s15
	s_nop 0
	v_addc_co_u32_e32 v31, vcc, 0, v3, vcc
	global_load_dwordx2 v[226:227], v[30:31], off
	global_load_dwordx2 v[228:229], v[30:31], off offset:512
	global_load_dwordx2 v[230:231], v[30:31], off offset:1024
	global_load_dwordx2 v[232:233], v[30:31], off offset:1536
	global_load_dwordx2 v[234:235], v[30:31], off offset:2048
	global_load_dwordx2 v[236:237], v[30:31], off offset:2560
	global_load_dwordx2 v[238:239], v[30:31], off offset:3072
	global_load_dwordx2 v[240:241], v[30:31], off offset:3584
	s_add_i32 s98, s22, 1
	s_ashr_i32 s99, s98, 31
	s_lshl_b64 s[98:99], s[98:99], 12
	v_lshl_add_u64 v[252:253], v[22:23], 0, s[98:99]
	global_load_dwordx2 v[242:243], v[252:253], off
	global_load_dwordx2 v[244:245], v[252:253], off offset:512
	global_load_dwordx2 v[246:247], v[252:253], off offset:1024
	global_load_dwordx2 v[248:249], v[252:253], off offset:1536
	global_load_dwordx2 v[250:251], v[252:253], off offset:2048
	s_ashr_i32 s0, s22, 13
	s_mulk_i32 s0, 0x3000
	s_ashr_i32 s1, s0, 31
	s_lshl_b64 s[0:1], s[0:1], 2
	s_add_u32 s20, s3, s0
	s_addc_u32 s21, s24, s1
	s_add_u32 s0, s20, 0x6000
	s_addc_u32 s1, s21, 0
	s_add_u32 s20, s20, 0x8000
	s_addc_u32 s21, s21, 0
	s_waitcnt vmcnt(12)
	v_and_b32_e32 v3, 0xffff0000, v226
	s_waitcnt vmcnt(11)
	v_and_b32_e32 v57, 0xffff0000, v228
	v_lshlrev_b32_e32 v2, 16, v226
	v_mul_f32_e32 v34, v3, v3
	v_lshlrev_b32_e32 v56, 16, v228
	v_mul_f32_e32 v32, v57, v57
	v_lshlrev_b32_e32 v4, 16, v227
	v_fmac_f32_e32 v34, v2, v2
	v_lshlrev_b32_e32 v58, 16, v229
	v_fmac_f32_e32 v32, v56, v56
	v_and_b32_e32 v5, 0xffff0000, v227
	v_fmac_f32_e32 v34, v4, v4
	v_and_b32_e32 v59, 0xffff0000, v229
	v_fmac_f32_e32 v32, v58, v58
	v_fmac_f32_e32 v34, v5, v5
	v_fmac_f32_e32 v32, v59, v59
	v_add_f32_e32 v34, v34, v32
	s_waitcnt vmcnt(10)
	v_and_b32_e32 v53, 0xffff0000, v230
	v_lshlrev_b32_e32 v52, 16, v230
	v_mul_f32_e32 v32, v53, v53
	v_lshlrev_b32_e32 v54, 16, v231
	v_fmac_f32_e32 v32, v52, v52
	v_and_b32_e32 v55, 0xffff0000, v231
	v_fmac_f32_e32 v32, v54, v54
	v_fmac_f32_e32 v32, v55, v55
	v_add_f32_e32 v34, v34, v32
	s_waitcnt vmcnt(9)
	v_and_b32_e32 v49, 0xffff0000, v232
	v_lshlrev_b32_e32 v48, 16, v232
	v_mul_f32_e32 v32, v49, v49
	v_lshlrev_b32_e32 v50, 16, v233
	v_fmac_f32_e32 v32, v48, v48
	v_and_b32_e32 v51, 0xffff0000, v233
	v_fmac_f32_e32 v32, v50, v50
	v_fmac_f32_e32 v32, v51, v51
	v_add_f32_e32 v36, v34, v32
	s_waitcnt vmcnt(8)
	v_and_b32_e32 v42, 0xffff0000, v234
	s_waitcnt vmcnt(7)
	v_and_b32_e32 v43, 0xffff0000, v236
	v_lshlrev_b32_e32 v41, 16, v236
	v_lshlrev_b32_e32 v40, 16, v234
	v_lshlrev_b32_e32 v44, 16, v235
	v_and_b32_e32 v46, 0xffff0000, v235
	v_pk_mul_f32 v[32:33], v[42:43], v[42:43]
	v_lshlrev_b32_e32 v45, 16, v237
	v_pk_fma_f32 v[32:33], v[40:41], v[40:41], v[32:33]
	v_and_b32_e32 v47, 0xffff0000, v237
	v_pk_fma_f32 v[32:33], v[44:45], v[44:45], v[32:33]
	s_nop 0
	v_pk_fma_f32 v[32:33], v[46:47], v[46:47], v[32:33]
	s_nop 0
	v_add_f32_e32 v32, v36, v32
	global_load_dwordx4 v[214:217], v202, s[0:1]
	global_load_dwordx4 v[218:221], v202, s[20:21]
	global_load_dwordx4 v[222:225], v[8:9], off
	v_add_f32_e32 v38, v32, v33
	s_waitcnt vmcnt(9)
	v_and_b32_e32 v32, 0xffff0000, v238
	s_waitcnt vmcnt(8)
	v_and_b32_e32 v33, 0xffff0000, v240
	v_lshlrev_b32_e32 v31, 16, v240
	v_lshlrev_b32_e32 v30, 16, v238
	v_lshlrev_b32_e32 v34, 16, v239
	v_and_b32_e32 v36, 0xffff0000, v239
	v_pk_mul_f32 v[60:61], v[32:33], v[32:33]
	v_lshlrev_b32_e32 v35, 16, v241
	v_pk_fma_f32 v[60:61], v[30:31], v[30:31], v[60:61]
	v_and_b32_e32 v37, 0xffff0000, v241
	v_pk_fma_f32 v[60:61], v[34:35], v[34:35], v[60:61]
	global_load_dwordx2 v[226:227], v[252:253], off offset:2560
	global_load_dwordx2 v[228:229], v[252:253], off offset:3072
	global_load_dwordx2 v[230:231], v[252:253], off offset:3584
	s_waitcnt vmcnt(4)
	v_pk_add_f32 v[218:219], v[218:219], 1.0 op_sel_hi:[1,0]
	v_pk_fma_f32 v[60:61], v[36:37], v[36:37], v[60:61]
	s_nop 0
	v_add_f32_e32 v38, v38, v60
	v_add_f32_e32 v38, v38, v61
	ds_bpermute_b32 v60, v189, v38
	s_waitcnt lgkmcnt(0)
	v_add_f32_e32 v38, v38, v60
	ds_bpermute_b32 v60, v192, v38
	s_waitcnt lgkmcnt(0)
	v_add_f32_e32 v38, v38, v60
	ds_bpermute_b32 v60, v193, v38
	s_waitcnt lgkmcnt(0)
	v_add_f32_e32 v38, v38, v60
	ds_bpermute_b32 v60, v194, v38
	s_waitcnt lgkmcnt(0)
	v_add_f32_e32 v38, v38, v60
	ds_bpermute_b32 v60, v195, v38
	s_waitcnt lgkmcnt(0)
	v_add_f32_e32 v38, v38, v60
	ds_bpermute_b32 v60, v196, v38
	s_waitcnt lgkmcnt(0)
	v_add_f32_e32 v38, v38, v60
	v_fmamk_f32 v38, v38, 0x3a000000, v201
	v_cmp_gt_f32_e32 vcc, s27, v38
	v_mul_f32_e32 v60, 0x4b800000, v38
	s_nop 0
	v_cndmask_b32_e32 v38, v38, v60, vcc
	v_rsq_f32_e32 v38, v38
	s_nop 0
	v_mul_f32_e32 v60, 0x45800000, v38
	v_cndmask_b32_e32 v38, v38, v60, vcc
	v_pk_mul_f32 v[2:3], v[2:3], v[38:39] op_sel_hi:[1,0]
	v_pk_mul_f32 v[4:5], v[4:5], v[38:39] op_sel_hi:[1,0]
	s_waitcnt vmcnt(3)
	v_pk_mul_f32 v[2:3], v[222:223], v[2:3]
	v_pk_mul_f32 v[4:5], v[224:225], v[4:5]
	v_pk_fma_f32 v[2:3], v[218:219], v[2:3], v[214:215]
	v_mov_b32_e32 v214, 0
	v_cvt_pk_fp8_f32 v214, v2, v3
	v_pk_add_f32 v[60:61], v[220:221], 1.0 op_sel_hi:[1,0]
	v_pk_mul_f32 v[56:57], v[56:57], v[38:39] op_sel_hi:[1,0]
	v_pk_fma_f32 v[4:5], v[60:61], v[4:5], v[216:217]
	v_lshl_add_u64 v[60:61], s[76:77], 0, v[26:27]
	v_cvt_pk_fp8_f32 v214, v4, v5 op_sel:[0,0,1]
	v_add_co_u32_e32 v60, vcc, s28, v60
	ds_write_b128 v199, v[2:5]
	s_nop 0
	v_addc_co_u32_e32 v61, vcc, 0, v61, vcc
	s_nop 1
	v_mov_b32_e32 v240, v214
	global_load_dwordx4 v[2:5], v203, s[0:1]
	s_nop 0
	global_load_dwordx4 v[214:217], v203, s[20:21]
	global_load_dwordx4 v[218:221], v[8:9], off offset:1024
	global_store_dword v[60:61], v240, off
	v_pk_mul_f32 v[58:59], v[58:59], v[38:39] op_sel_hi:[1,0]
	v_pk_mul_f32 v[52:53], v[52:53], v[38:39] op_sel_hi:[1,0]
	v_pk_mul_f32 v[54:55], v[54:55], v[38:39] op_sel_hi:[1,0]
	v_pk_mul_f32 v[48:49], v[48:49], v[38:39] op_sel_hi:[1,0]
	v_pk_mul_f32 v[50:51], v[50:51], v[38:39] op_sel_hi:[1,0]
	s_waitcnt vmcnt(2)
	v_pk_add_f32 v[214:215], v[214:215], 1.0 op_sel_hi:[1,0]
	s_waitcnt vmcnt(1)
	v_pk_mul_f32 v[56:57], v[218:219], v[56:57]
	v_pk_mul_f32 v[58:59], v[220:221], v[58:59]
	v_pk_fma_f32 v[2:3], v[214:215], v[56:57], v[2:3]
	v_mov_b32_e32 v56, 0
	v_cvt_pk_fp8_f32 v56, v2, v3
	v_pk_add_f32 v[216:217], v[216:217], 1.0 op_sel_hi:[1,0]
	s_nop 0
	v_pk_fma_f32 v[4:5], v[216:217], v[58:59], v[4:5]
	ds_write_b128 v199, v[2:5] offset:1024
	v_cvt_pk_fp8_f32 v56, v4, v5 op_sel:[0,0,1]
	s_nop 1
	v_mov_b32_e32 v240, v56
	global_load_dwordx4 v[2:5], v204, s[0:1]
	s_nop 0
	global_load_dwordx4 v[56:59], v204, s[20:21]
	global_load_dwordx4 v[214:217], v[8:9], off offset:2048
	global_store_dword v[60:61], v240, off offset:256
	s_waitcnt vmcnt(2)
	v_pk_add_f32 v[56:57], v[56:57], 1.0 op_sel_hi:[1,0]
	s_waitcnt vmcnt(1)
	v_pk_mul_f32 v[52:53], v[214:215], v[52:53]
	v_pk_mul_f32 v[54:55], v[216:217], v[54:55]
	v_pk_fma_f32 v[2:3], v[56:57], v[52:53], v[2:3]
	v_mov_b32_e32 v52, 0
	v_cvt_pk_fp8_f32 v52, v2, v3
	v_pk_add_f32 v[58:59], v[58:59], 1.0 op_sel_hi:[1,0]
	s_nop 0
	v_pk_fma_f32 v[4:5], v[58:59], v[54:55], v[4:5]
	ds_write_b128 v199, v[2:5] offset:2048
	v_cvt_pk_fp8_f32 v52, v4, v5 op_sel:[0,0,1]
	s_nop 1
	v_mov_b32_e32 v240, v52
	global_load_dwordx4 v[2:5], v205, s[0:1]
	s_nop 0
	global_load_dwordx4 v[52:55], v205, s[20:21]
	global_load_dwordx4 v[56:59], v[8:9], off offset:3072
	global_store_dword v[60:61], v240, off offset:512
	s_waitcnt vmcnt(2)
	v_pk_add_f32 v[52:53], v[52:53], 1.0 op_sel_hi:[1,0]
	s_waitcnt vmcnt(1)
	v_pk_mul_f32 v[48:49], v[48:49], v[56:57]
	v_pk_mul_f32 v[50:51], v[50:51], v[58:59]
	v_pk_fma_f32 v[2:3], v[52:53], v[48:49], v[2:3]
	v_mov_b32_e32 v48, 0
	v_cvt_pk_fp8_f32 v48, v2, v3
	v_pk_add_f32 v[54:55], v[54:55], 1.0 op_sel_hi:[1,0]
	v_mov_b32_e32 v58, v40
	v_pk_fma_f32 v[4:5], v[54:55], v[50:51], v[4:5]
	ds_write_b128 v199, v[2:5] offset:3072
	v_cvt_pk_fp8_f32 v48, v4, v5 op_sel:[0,0,1]
	v_mov_b32_e32 v59, v42
	v_pk_mul_f32 v[58:59], v[58:59], v[38:39] op_sel_hi:[1,0]
	v_mov_b32_e32 v40, 0
	s_nop 1
	v_mov_b32_e32 v240, v48
	global_load_dwordx4 v[2:5], v206, s[0:1]
	s_nop 0
	global_load_dwordx4 v[48:51], v206, s[20:21]
	global_load_dwordx4 v[52:55], v[10:11], off
	global_store_dword v[60:61], v240, off offset:768
	v_mov_b32_e32 v56, v44
	v_mov_b32_e32 v57, v46
	v_pk_mul_f32 v[56:57], v[56:57], v[38:39] op_sel_hi:[1,0]
	v_mov_b32_e32 v42, v41
	v_mov_b32_e32 v46, v45
	v_pk_mul_f32 v[44:45], v[46:47], v[38:39] op_sel_hi:[1,0]
	s_waitcnt vmcnt(2)
	v_pk_add_f32 v[48:49], v[48:49], 1.0 op_sel_hi:[1,0]
	s_waitcnt vmcnt(1)
	v_pk_mul_f32 v[52:53], v[58:59], v[52:53]
	v_pk_mul_f32 v[54:55], v[56:57], v[54:55]
	v_pk_fma_f32 v[2:3], v[48:49], v[52:53], v[2:3]
	v_pk_add_f32 v[50:51], v[50:51], 1.0 op_sel_hi:[1,0]
	v_cvt_pk_fp8_f32 v40, v2, v3
	v_pk_fma_f32 v[4:5], v[50:51], v[54:55], v[4:5]
	ds_write_b128 v199, v[2:5] offset:4096
	v_cvt_pk_fp8_f32 v40, v4, v5 op_sel:[0,0,1]
	s_nop 1
	v_mov_b32_e32 v240, v40
	global_load_dwordx4 v[2:5], v207, s[0:1]
	global_load_dwordx4 v[48:51], v207, s[20:21]
	global_load_dwordx4 v[52:55], v[12:13], off
	global_store_dword v[60:61], v240, off offset:1024
	v_pk_mul_f32 v[40:41], v[42:43], v[38:39] op_sel_hi:[1,0]
	s_waitcnt vmcnt(2)
	v_pk_add_f32 v[46:47], v[48:49], 1.0 op_sel_hi:[1,0]
	s_waitcnt vmcnt(1)
	v_pk_mul_f32 v[40:41], v[40:41], v[52:53]
	v_pk_mul_f32 v[42:43], v[44:45], v[54:55]
	v_pk_fma_f32 v[2:3], v[46:47], v[40:41], v[2:3]
	v_mov_b32_e32 v40, 0
	v_cvt_pk_fp8_f32 v40, v2, v3
	v_pk_add_f32 v[44:45], v[50:51], 1.0 op_sel_hi:[1,0]
	v_mov_b32_e32 v50, v30
	v_pk_fma_f32 v[4:5], v[44:45], v[42:43], v[4:5]
	ds_write_b128 v199, v[2:5] offset:5120
	v_cvt_pk_fp8_f32 v40, v4, v5 op_sel:[0,0,1]
	v_mov_b32_e32 v51, v32
	v_pk_mul_f32 v[50:51], v[50:51], v[38:39] op_sel_hi:[1,0]
	v_mov_b32_e32 v30, 0
	s_nop 1
	v_mov_b32_e32 v240, v40
	global_load_dwordx4 v[2:5], v208, s[0:1]
	s_nop 0
	global_load_dwordx4 v[40:43], v208, s[20:21]
	global_load_dwordx4 v[44:47], v[14:15], off
	global_store_dword v[60:61], v240, off offset:1280
	v_mov_b32_e32 v48, v34
	v_mov_b32_e32 v49, v36
	v_pk_mul_f32 v[48:49], v[48:49], v[38:39] op_sel_hi:[1,0]
	v_mov_b32_e32 v32, v31
	v_mov_b32_e32 v36, v35
	v_pk_mul_f32 v[34:35], v[36:37], v[38:39] op_sel_hi:[1,0]
	s_waitcnt vmcnt(2)
	v_pk_add_f32 v[40:41], v[40:41], 1.0 op_sel_hi:[1,0]
	s_waitcnt vmcnt(1)
	v_pk_mul_f32 v[44:45], v[50:51], v[44:45]
	v_pk_mul_f32 v[46:47], v[48:49], v[46:47]
	v_pk_fma_f32 v[2:3], v[40:41], v[44:45], v[2:3]
	v_pk_add_f32 v[42:43], v[42:43], 1.0 op_sel_hi:[1,0]
	v_cvt_pk_fp8_f32 v30, v2, v3
	v_pk_fma_f32 v[4:5], v[42:43], v[46:47], v[4:5]
	ds_write_b128 v199, v[2:5] offset:6144
	v_cvt_pk_fp8_f32 v30, v4, v5 op_sel:[0,0,1]
	s_nop 1
	v_mov_b32_e32 v240, v30
	global_load_dwordx4 v[2:5], v209, s[0:1]
	global_load_dwordx4 v[40:43], v209, s[20:21]
	global_load_dwordx4 v[44:47], v[16:17], off
	global_store_dword v[60:61], v240, off offset:1536
	v_pk_mul_f32 v[30:31], v[32:33], v[38:39] op_sel_hi:[1,0]
	s_add_i32 s0, s22, 1
	s_ashr_i32 s1, s0, 31
	s_lshl_b64 s[20:21], s[0:1], 12
	s_lshl_b64 s[22:23], s[0:1], 11
	s_ashr_i32 s0, s0, 13
	s_mulk_i32 s0, 0x3000
	s_ashr_i32 s1, s0, 31
	s_lshl_b64 s[0:1], s[0:1], 2
	s_waitcnt vmcnt(2)
	v_pk_add_f32 v[36:37], v[40:41], 1.0 op_sel_hi:[1,0]
	s_waitcnt vmcnt(1)
	v_pk_mul_f32 v[30:31], v[30:31], v[44:45]
	v_pk_mul_f32 v[32:33], v[34:35], v[46:47]
	v_pk_fma_f32 v[2:3], v[36:37], v[30:31], v[2:3]
	v_mov_b32_e32 v30, 0
	v_cvt_pk_fp8_f32 v30, v2, v3
	v_pk_add_f32 v[34:35], v[42:43], 1.0 op_sel_hi:[1,0]
	s_nop 0
	v_pk_fma_f32 v[4:5], v[34:35], v[32:33], v[4:5]
	ds_write_b128 v199, v[2:5] offset:7168
	v_cvt_pk_fp8_f32 v30, v4, v5 op_sel:[0,0,1]
	global_store_dword v[60:61], v30, off offset:1792
	v_lshl_add_u64 v[30:31], v[22:23], 0, s[20:21]
	s_add_u32 s20, s3, s0
	s_addc_u32 s21, s24, s1
	s_add_u32 s0, s20, 0x6000
	s_addc_u32 s1, s21, 0
	s_add_u32 s20, s20, 0x8000
	s_addc_u32 s21, s21, 0
	v_and_b32_e32 v3, 0xffff0000, v242
	v_and_b32_e32 v57, 0xffff0000, v244
	v_lshlrev_b32_e32 v2, 16, v242
	v_mul_f32_e32 v34, v3, v3
	v_lshlrev_b32_e32 v56, 16, v244
	v_mul_f32_e32 v32, v57, v57
	v_lshlrev_b32_e32 v4, 16, v243
	v_fmac_f32_e32 v34, v2, v2
	v_lshlrev_b32_e32 v58, 16, v245
	v_fmac_f32_e32 v32, v56, v56
	v_and_b32_e32 v5, 0xffff0000, v243
	v_fmac_f32_e32 v34, v4, v4
	v_and_b32_e32 v59, 0xffff0000, v245
	v_fmac_f32_e32 v32, v58, v58
	v_fmac_f32_e32 v34, v5, v5
	v_fmac_f32_e32 v32, v59, v59
	v_add_f32_e32 v34, v34, v32
	v_and_b32_e32 v53, 0xffff0000, v246
	v_lshlrev_b32_e32 v52, 16, v246
	v_mul_f32_e32 v32, v53, v53
	v_lshlrev_b32_e32 v54, 16, v247
	v_fmac_f32_e32 v32, v52, v52
	v_and_b32_e32 v55, 0xffff0000, v247
	v_fmac_f32_e32 v32, v54, v54
	v_fmac_f32_e32 v32, v55, v55
	v_add_f32_e32 v34, v34, v32
	v_and_b32_e32 v49, 0xffff0000, v248
	v_lshlrev_b32_e32 v48, 16, v248
	v_mul_f32_e32 v32, v49, v49
	v_lshlrev_b32_e32 v50, 16, v249
	v_fmac_f32_e32 v32, v48, v48
	v_and_b32_e32 v51, 0xffff0000, v249
	v_fmac_f32_e32 v32, v50, v50
	v_fmac_f32_e32 v32, v51, v51
	v_add_f32_e32 v36, v34, v32
	v_and_b32_e32 v42, 0xffff0000, v250
	v_and_b32_e32 v43, 0xffff0000, v226
	v_lshlrev_b32_e32 v41, 16, v226
	v_lshlrev_b32_e32 v40, 16, v250
	v_lshlrev_b32_e32 v44, 16, v251
	v_and_b32_e32 v46, 0xffff0000, v251
	v_pk_mul_f32 v[32:33], v[42:43], v[42:43]
	v_lshlrev_b32_e32 v45, 16, v227
	v_pk_fma_f32 v[32:33], v[40:41], v[40:41], v[32:33]
	v_and_b32_e32 v47, 0xffff0000, v227
	v_pk_fma_f32 v[32:33], v[44:45], v[44:45], v[32:33]
	s_nop 0
	v_pk_fma_f32 v[32:33], v[46:47], v[46:47], v[32:33]
	s_nop 0
	v_add_f32_e32 v32, v36, v32
	global_load_dwordx4 v[214:217], v202, s[0:1]
	global_load_dwordx4 v[218:221], v202, s[20:21]
	global_load_dwordx4 v[222:225], v[8:9], off
	v_add_f32_e32 v38, v32, v33
	s_waitcnt vmcnt(4)
	v_and_b32_e32 v32, 0xffff0000, v228
	s_waitcnt vmcnt(3)
	v_and_b32_e32 v33, 0xffff0000, v230
	v_lshlrev_b32_e32 v31, 16, v230
	v_lshlrev_b32_e32 v30, 16, v228
	v_lshlrev_b32_e32 v34, 16, v229
	v_and_b32_e32 v36, 0xffff0000, v229
	v_pk_mul_f32 v[60:61], v[32:33], v[32:33]
	v_lshlrev_b32_e32 v35, 16, v231
	v_pk_fma_f32 v[60:61], v[30:31], v[30:31], v[60:61]
	v_and_b32_e32 v37, 0xffff0000, v231
	v_pk_fma_f32 v[60:61], v[34:35], v[34:35], v[60:61]
	s_waitcnt vmcnt(1)
	v_pk_add_f32 v[218:219], v[218:219], 1.0 op_sel_hi:[1,0]
	v_pk_fma_f32 v[60:61], v[36:37], v[36:37], v[60:61]
	s_nop 0
	v_add_f32_e32 v38, v38, v60
	v_add_f32_e32 v38, v38, v61
	ds_bpermute_b32 v60, v189, v38
	s_waitcnt lgkmcnt(0)
	v_add_f32_e32 v38, v38, v60
	ds_bpermute_b32 v60, v192, v38
	s_waitcnt lgkmcnt(0)
	v_add_f32_e32 v38, v38, v60
	ds_bpermute_b32 v60, v193, v38
	s_waitcnt lgkmcnt(0)
	v_add_f32_e32 v38, v38, v60
	ds_bpermute_b32 v60, v194, v38
	s_waitcnt lgkmcnt(0)
	v_add_f32_e32 v38, v38, v60
	ds_bpermute_b32 v60, v195, v38
	s_waitcnt lgkmcnt(0)
	v_add_f32_e32 v38, v38, v60
	ds_bpermute_b32 v60, v196, v38
	s_waitcnt lgkmcnt(0)
	v_add_f32_e32 v38, v38, v60
	v_fmamk_f32 v38, v38, 0x3a000000, v201
	v_cmp_gt_f32_e32 vcc, s27, v38
	v_mul_f32_e32 v60, 0x4b800000, v38
	s_nop 0
	v_cndmask_b32_e32 v38, v38, v60, vcc
	v_rsq_f32_e32 v38, v38
	s_nop 0
	v_mul_f32_e32 v60, 0x45800000, v38
	v_cndmask_b32_e32 v38, v38, v60, vcc
	v_pk_mul_f32 v[2:3], v[2:3], v[38:39] op_sel_hi:[1,0]
	v_pk_mul_f32 v[4:5], v[4:5], v[38:39] op_sel_hi:[1,0]
	s_waitcnt vmcnt(0)
	v_pk_mul_f32 v[2:3], v[222:223], v[2:3]
	v_pk_mul_f32 v[4:5], v[224:225], v[4:5]
	v_pk_fma_f32 v[2:3], v[218:219], v[2:3], v[214:215]
	v_mov_b32_e32 v214, 0
	v_cvt_pk_fp8_f32 v214, v2, v3
	v_pk_add_f32 v[60:61], v[220:221], 1.0 op_sel_hi:[1,0]
	v_pk_mul_f32 v[56:57], v[56:57], v[38:39] op_sel_hi:[1,0]
	v_pk_fma_f32 v[4:5], v[60:61], v[4:5], v[216:217]
	v_lshl_add_u64 v[60:61], v[24:25], 0, s[22:23]
	v_cvt_pk_fp8_f32 v214, v4, v5 op_sel:[0,0,1]
	ds_write_b128 v200, v[2:5]
	v_pk_mul_f32 v[58:59], v[58:59], v[38:39] op_sel_hi:[1,0]
	v_pk_mul_f32 v[52:53], v[52:53], v[38:39] op_sel_hi:[1,0]
	s_nop 1
	v_mov_b32_e32 v240, v214
	global_load_dwordx4 v[2:5], v203, s[0:1]
	s_nop 0
	global_load_dwordx4 v[214:217], v203, s[20:21]
	global_load_dwordx4 v[218:221], v[8:9], off offset:1024
	global_store_dword v[60:61], v240, off
	v_pk_mul_f32 v[54:55], v[54:55], v[38:39] op_sel_hi:[1,0]
	v_pk_mul_f32 v[48:49], v[48:49], v[38:39] op_sel_hi:[1,0]
	v_pk_mul_f32 v[50:51], v[50:51], v[38:39] op_sel_hi:[1,0]
	s_waitcnt vmcnt(2)
	v_pk_add_f32 v[214:215], v[214:215], 1.0 op_sel_hi:[1,0]
	s_waitcnt vmcnt(1)
	v_pk_mul_f32 v[56:57], v[218:219], v[56:57]
	v_pk_mul_f32 v[58:59], v[220:221], v[58:59]
	v_pk_fma_f32 v[2:3], v[214:215], v[56:57], v[2:3]
	v_mov_b32_e32 v56, 0
	v_cvt_pk_fp8_f32 v56, v2, v3
	v_pk_add_f32 v[216:217], v[216:217], 1.0 op_sel_hi:[1,0]
	s_nop 0
	v_pk_fma_f32 v[4:5], v[216:217], v[58:59], v[4:5]
	ds_write_b128 v200, v[2:5] offset:1024
	v_cvt_pk_fp8_f32 v56, v4, v5 op_sel:[0,0,1]
	s_nop 1
	v_mov_b32_e32 v240, v56
	global_load_dwordx4 v[2:5], v204, s[0:1]
	s_nop 0
	global_load_dwordx4 v[56:59], v204, s[20:21]
	global_load_dwordx4 v[214:217], v[8:9], off offset:2048
	global_store_dword v[60:61], v240, off offset:256
	s_waitcnt vmcnt(2)
	v_pk_add_f32 v[56:57], v[56:57], 1.0 op_sel_hi:[1,0]
	s_waitcnt vmcnt(1)
	v_pk_mul_f32 v[52:53], v[214:215], v[52:53]
	v_pk_mul_f32 v[54:55], v[216:217], v[54:55]
	v_pk_fma_f32 v[2:3], v[56:57], v[52:53], v[2:3]
	v_mov_b32_e32 v52, 0
	v_cvt_pk_fp8_f32 v52, v2, v3
	v_pk_add_f32 v[58:59], v[58:59], 1.0 op_sel_hi:[1,0]
	s_nop 0
	v_pk_fma_f32 v[4:5], v[58:59], v[54:55], v[4:5]
	ds_write_b128 v200, v[2:5] offset:2048
	v_cvt_pk_fp8_f32 v52, v4, v5 op_sel:[0,0,1]
	s_nop 1
	v_mov_b32_e32 v240, v52
	global_load_dwordx4 v[2:5], v205, s[0:1]
	s_nop 0
	global_load_dwordx4 v[52:55], v205, s[20:21]
	global_load_dwordx4 v[56:59], v[8:9], off offset:3072
	global_store_dword v[60:61], v240, off offset:512
	s_waitcnt vmcnt(2)
	v_pk_add_f32 v[52:53], v[52:53], 1.0 op_sel_hi:[1,0]
	s_waitcnt vmcnt(1)
	v_pk_mul_f32 v[48:49], v[48:49], v[56:57]
	v_pk_mul_f32 v[50:51], v[50:51], v[58:59]
	v_pk_fma_f32 v[2:3], v[52:53], v[48:49], v[2:3]
	v_mov_b32_e32 v48, 0
	v_cvt_pk_fp8_f32 v48, v2, v3
	v_pk_add_f32 v[54:55], v[54:55], 1.0 op_sel_hi:[1,0]
	v_mov_b32_e32 v58, v40
	v_pk_fma_f32 v[4:5], v[54:55], v[50:51], v[4:5]
	ds_write_b128 v200, v[2:5] offset:3072
	v_cvt_pk_fp8_f32 v48, v4, v5 op_sel:[0,0,1]
	v_mov_b32_e32 v59, v42
	v_pk_mul_f32 v[58:59], v[58:59], v[38:39] op_sel_hi:[1,0]
	v_mov_b32_e32 v40, 0
	s_nop 1
	v_mov_b32_e32 v240, v48
	global_load_dwordx4 v[2:5], v206, s[0:1]
	s_nop 0
	global_load_dwordx4 v[48:51], v206, s[20:21]
	global_load_dwordx4 v[52:55], v[10:11], off
	global_store_dword v[60:61], v240, off offset:768
	v_mov_b32_e32 v56, v44
	v_mov_b32_e32 v57, v46
	v_pk_mul_f32 v[56:57], v[56:57], v[38:39] op_sel_hi:[1,0]
	v_mov_b32_e32 v42, v41
	v_mov_b32_e32 v46, v45
	v_pk_mul_f32 v[44:45], v[46:47], v[38:39] op_sel_hi:[1,0]
	s_waitcnt vmcnt(2)
	v_pk_add_f32 v[48:49], v[48:49], 1.0 op_sel_hi:[1,0]
	s_waitcnt vmcnt(1)
	v_pk_mul_f32 v[52:53], v[58:59], v[52:53]
	v_pk_mul_f32 v[54:55], v[56:57], v[54:55]
	v_pk_fma_f32 v[2:3], v[48:49], v[52:53], v[2:3]
	v_pk_add_f32 v[50:51], v[50:51], 1.0 op_sel_hi:[1,0]
	v_cvt_pk_fp8_f32 v40, v2, v3
	v_pk_fma_f32 v[4:5], v[50:51], v[54:55], v[4:5]
	ds_write_b128 v200, v[2:5] offset:4096
	v_cvt_pk_fp8_f32 v40, v4, v5 op_sel:[0,0,1]
	s_nop 1
	v_mov_b32_e32 v240, v40
	global_load_dwordx4 v[2:5], v207, s[0:1]
	global_load_dwordx4 v[48:51], v207, s[20:21]
	global_load_dwordx4 v[52:55], v[12:13], off
	global_store_dword v[60:61], v240, off offset:1024
	v_pk_mul_f32 v[40:41], v[42:43], v[38:39] op_sel_hi:[1,0]
	s_waitcnt vmcnt(2)
	v_pk_add_f32 v[46:47], v[48:49], 1.0 op_sel_hi:[1,0]
	s_waitcnt vmcnt(1)
	v_pk_mul_f32 v[40:41], v[40:41], v[52:53]
	v_pk_mul_f32 v[42:43], v[44:45], v[54:55]
	v_pk_fma_f32 v[2:3], v[46:47], v[40:41], v[2:3]
	v_mov_b32_e32 v40, 0
	v_cvt_pk_fp8_f32 v40, v2, v3
	v_pk_add_f32 v[44:45], v[50:51], 1.0 op_sel_hi:[1,0]
	v_mov_b32_e32 v50, v30
	v_pk_fma_f32 v[4:5], v[44:45], v[42:43], v[4:5]
	ds_write_b128 v200, v[2:5] offset:5120
	v_cvt_pk_fp8_f32 v40, v4, v5 op_sel:[0,0,1]
	v_mov_b32_e32 v51, v32
	v_pk_mul_f32 v[50:51], v[50:51], v[38:39] op_sel_hi:[1,0]
	v_mov_b32_e32 v30, 0
	s_nop 1
	v_mov_b32_e32 v240, v40
	global_load_dwordx4 v[2:5], v208, s[0:1]
	s_nop 0
	global_load_dwordx4 v[40:43], v208, s[20:21]
	global_load_dwordx4 v[44:47], v[14:15], off
	global_store_dword v[60:61], v240, off offset:1280
	v_mov_b32_e32 v48, v34
	v_mov_b32_e32 v49, v36
	v_pk_mul_f32 v[48:49], v[48:49], v[38:39] op_sel_hi:[1,0]
	v_mov_b32_e32 v32, v31
	v_mov_b32_e32 v36, v35
	v_pk_mul_f32 v[34:35], v[36:37], v[38:39] op_sel_hi:[1,0]
	s_waitcnt vmcnt(2)
	v_pk_add_f32 v[40:41], v[40:41], 1.0 op_sel_hi:[1,0]
	s_waitcnt vmcnt(1)
	v_pk_mul_f32 v[44:45], v[50:51], v[44:45]
	v_pk_mul_f32 v[46:47], v[48:49], v[46:47]
	v_pk_fma_f32 v[2:3], v[40:41], v[44:45], v[2:3]
	v_pk_add_f32 v[42:43], v[42:43], 1.0 op_sel_hi:[1,0]
	v_cvt_pk_fp8_f32 v30, v2, v3
	v_pk_fma_f32 v[4:5], v[42:43], v[46:47], v[4:5]
	ds_write_b128 v200, v[2:5] offset:6144
	v_cvt_pk_fp8_f32 v30, v4, v5 op_sel:[0,0,1]
	s_nop 1
	v_mov_b32_e32 v240, v30
	global_load_dwordx4 v[2:5], v209, s[0:1]
	global_load_dwordx4 v[40:43], v209, s[20:21]
	global_load_dwordx4 v[44:47], v[16:17], off
	global_store_dword v[60:61], v240, off offset:1536
	v_pk_mul_f32 v[30:31], v[32:33], v[38:39] op_sel_hi:[1,0]
	s_waitcnt vmcnt(2)
	v_pk_add_f32 v[36:37], v[40:41], 1.0 op_sel_hi:[1,0]
	s_waitcnt vmcnt(1)
	v_pk_mul_f32 v[30:31], v[30:31], v[44:45]
	v_pk_mul_f32 v[32:33], v[34:35], v[46:47]
	v_pk_fma_f32 v[2:3], v[36:37], v[30:31], v[2:3]
	v_mov_b32_e32 v30, 0
	v_cvt_pk_fp8_f32 v30, v2, v3
	v_pk_add_f32 v[34:35], v[42:43], 1.0 op_sel_hi:[1,0]
	s_nop 0
	v_pk_fma_f32 v[4:5], v[34:35], v[32:33], v[4:5]
	ds_write_b128 v200, v[2:5] offset:7168
	v_cvt_pk_fp8_f32 v30, v4, v5 op_sel:[0,0,1]
	global_store_dword v[60:61], v30, off offset:1792
	s_waitcnt lgkmcnt(0)
	s_barrier
	ds_read_b128 v[2:5], v210
	s_waitcnt lgkmcnt(0)
	v_mfma_f32_16x16x4_f32 v[30:33], v2, v1, 0
	v_mfma_f32_16x16x4_f32 v[34:37], v2, v39, 0
	v_mfma_f32_16x16x4_f32 v[30:33], v3, v62, v[30:33]
	v_mfma_f32_16x16x4_f32 v[34:37], v3, v63, v[34:37]
	v_mfma_f32_16x16x4_f32 v[30:33], v4, v64, v[30:33]
	v_mfma_f32_16x16x4_f32 v[34:37], v4, v65, v[34:37]
	v_mfma_f32_16x16x4_f32 v[30:33], v5, v66, v[30:33]
	v_mfma_f32_16x16x4_f32 v[2:5], v5, v67, v[34:37]
	s_nop 7
	ds_read_b128 v[34:37], v210 offset:64
	s_waitcnt lgkmcnt(0)
	v_mfma_f32_16x16x4_f32 v[30:33], v34, v68, v[30:33]
	v_mfma_f32_16x16x4_f32 v[2:5], v34, v69, v[2:5]
	v_mfma_f32_16x16x4_f32 v[30:33], v35, v70, v[30:33]
	v_mfma_f32_16x16x4_f32 v[2:5], v35, v71, v[2:5]
	v_mfma_f32_16x16x4_f32 v[30:33], v36, v72, v[30:33]
	v_mfma_f32_16x16x4_f32 v[2:5], v36, v73, v[2:5]
	v_mfma_f32_16x16x4_f32 v[30:33], v37, v74, v[30:33]
	v_mfma_f32_16x16x4_f32 v[2:5], v37, v75, v[2:5]
	ds_read_b128 v[34:37], v210 offset:128
	s_waitcnt lgkmcnt(0)
	v_mfma_f32_16x16x4_f32 v[30:33], v34, v76, v[30:33]
	v_mfma_f32_16x16x4_f32 v[2:5], v34, v77, v[2:5]
	v_mfma_f32_16x16x4_f32 v[30:33], v35, v78, v[30:33]
	v_mfma_f32_16x16x4_f32 v[2:5], v35, v79, v[2:5]
	v_mfma_f32_16x16x4_f32 v[30:33], v36, v80, v[30:33]
	v_mfma_f32_16x16x4_f32 v[2:5], v36, v81, v[2:5]
	v_mfma_f32_16x16x4_f32 v[30:33], v37, v82, v[30:33]
	v_mfma_f32_16x16x4_f32 v[2:5], v37, v83, v[2:5]
	ds_read_b128 v[34:37], v210 offset:192
	s_waitcnt lgkmcnt(0)
	v_mfma_f32_16x16x4_f32 v[30:33], v34, v84, v[30:33]
	v_mfma_f32_16x16x4_f32 v[2:5], v34, v85, v[2:5]
	v_mfma_f32_16x16x4_f32 v[30:33], v35, v86, v[30:33]
	v_mfma_f32_16x16x4_f32 v[2:5], v35, v87, v[2:5]
	v_mfma_f32_16x16x4_f32 v[30:33], v36, v88, v[30:33]
	v_mfma_f32_16x16x4_f32 v[2:5], v36, v89, v[2:5]
	v_mfma_f32_16x16x4_f32 v[30:33], v37, v90, v[30:33]
	v_mfma_f32_16x16x4_f32 v[2:5], v37, v91, v[2:5]
	ds_read_b128 v[34:37], v210 offset:256
	s_waitcnt lgkmcnt(0)
	v_mfma_f32_16x16x4_f32 v[30:33], v34, v92, v[30:33]
	v_mfma_f32_16x16x4_f32 v[2:5], v34, v93, v[2:5]
	v_mfma_f32_16x16x4_f32 v[30:33], v35, v94, v[30:33]
	v_mfma_f32_16x16x4_f32 v[2:5], v35, v95, v[2:5]
	v_mfma_f32_16x16x4_f32 v[30:33], v36, v96, v[30:33]
	v_mfma_f32_16x16x4_f32 v[2:5], v36, v97, v[2:5]
	v_mfma_f32_16x16x4_f32 v[30:33], v37, v98, v[30:33]
	v_mfma_f32_16x16x4_f32 v[2:5], v37, v99, v[2:5]
	ds_read_b128 v[34:37], v210 offset:320
	s_waitcnt lgkmcnt(0)
	v_mfma_f32_16x16x4_f32 v[30:33], v34, v100, v[30:33]
	v_mfma_f32_16x16x4_f32 v[2:5], v34, v101, v[2:5]
	v_mfma_f32_16x16x4_f32 v[30:33], v35, v102, v[30:33]
	v_mfma_f32_16x16x4_f32 v[2:5], v35, v103, v[2:5]
	v_mfma_f32_16x16x4_f32 v[30:33], v36, v104, v[30:33]
	v_mfma_f32_16x16x4_f32 v[2:5], v36, v105, v[2:5]
	v_mfma_f32_16x16x4_f32 v[30:33], v37, v106, v[30:33]
	v_mfma_f32_16x16x4_f32 v[2:5], v37, v107, v[2:5]
	ds_read_b128 v[34:37], v210 offset:384
	s_waitcnt lgkmcnt(0)
	v_mfma_f32_16x16x4_f32 v[30:33], v34, v108, v[30:33]
	v_mfma_f32_16x16x4_f32 v[2:5], v34, v109, v[2:5]
	v_mfma_f32_16x16x4_f32 v[30:33], v35, v110, v[30:33]
	v_mfma_f32_16x16x4_f32 v[2:5], v35, v111, v[2:5]
	v_mfma_f32_16x16x4_f32 v[30:33], v36, v112, v[30:33]
	v_mfma_f32_16x16x4_f32 v[2:5], v36, v113, v[2:5]
	v_mfma_f32_16x16x4_f32 v[30:33], v37, v114, v[30:33]
	v_mfma_f32_16x16x4_f32 v[2:5], v37, v115, v[2:5]
	ds_read_b128 v[34:37], v210 offset:448
	s_waitcnt lgkmcnt(0)
	v_mfma_f32_16x16x4_f32 v[30:33], v34, v116, v[30:33]
	v_mfma_f32_16x16x4_f32 v[2:5], v34, v117, v[2:5]
	v_mfma_f32_16x16x4_f32 v[30:33], v35, v118, v[30:33]
	v_mfma_f32_16x16x4_f32 v[2:5], v35, v119, v[2:5]
	v_mfma_f32_16x16x4_f32 v[30:33], v36, v120, v[30:33]
	v_mfma_f32_16x16x4_f32 v[2:5], v36, v121, v[2:5]
	v_mfma_f32_16x16x4_f32 v[30:33], v37, v122, v[30:33]
	v_mfma_f32_16x16x4_f32 v[2:5], v37, v123, v[2:5]
	ds_read_b128 v[34:37], v210 offset:512
	s_waitcnt lgkmcnt(0)
	v_mfma_f32_16x16x4_f32 v[30:33], v34, v124, v[30:33]
	v_mfma_f32_16x16x4_f32 v[2:5], v34, v125, v[2:5]
	v_mfma_f32_16x16x4_f32 v[30:33], v35, v126, v[30:33]
	v_mfma_f32_16x16x4_f32 v[2:5], v35, v127, v[2:5]
	v_mfma_f32_16x16x4_f32 v[30:33], v36, v128, v[30:33]
	v_mfma_f32_16x16x4_f32 v[2:5], v36, v129, v[2:5]
	v_mfma_f32_16x16x4_f32 v[30:33], v37, v130, v[30:33]
	v_mfma_f32_16x16x4_f32 v[2:5], v37, v131, v[2:5]
	ds_read_b128 v[34:37], v210 offset:576
	s_waitcnt lgkmcnt(0)
	v_mfma_f32_16x16x4_f32 v[30:33], v34, v132, v[30:33]
	v_mfma_f32_16x16x4_f32 v[2:5], v34, v133, v[2:5]
	v_mfma_f32_16x16x4_f32 v[30:33], v35, v134, v[30:33]
	v_mfma_f32_16x16x4_f32 v[2:5], v35, v135, v[2:5]
	v_mfma_f32_16x16x4_f32 v[30:33], v36, v136, v[30:33]
	v_mfma_f32_16x16x4_f32 v[2:5], v36, v137, v[2:5]
	v_mfma_f32_16x16x4_f32 v[30:33], v37, v138, v[30:33]
	v_mfma_f32_16x16x4_f32 v[2:5], v37, v139, v[2:5]
	ds_read_b128 v[34:37], v210 offset:640
	s_waitcnt lgkmcnt(0)
	v_mfma_f32_16x16x4_f32 v[30:33], v34, v140, v[30:33]
	v_mfma_f32_16x16x4_f32 v[2:5], v34, v141, v[2:5]
	v_mfma_f32_16x16x4_f32 v[30:33], v35, v142, v[30:33]
	v_mfma_f32_16x16x4_f32 v[2:5], v35, v143, v[2:5]
	v_mfma_f32_16x16x4_f32 v[30:33], v36, v144, v[30:33]
	v_mfma_f32_16x16x4_f32 v[2:5], v36, v145, v[2:5]
	v_mfma_f32_16x16x4_f32 v[30:33], v37, v146, v[30:33]
	v_mfma_f32_16x16x4_f32 v[2:5], v37, v147, v[2:5]
	ds_read_b128 v[34:37], v210 offset:704
	s_waitcnt lgkmcnt(0)
	v_mfma_f32_16x16x4_f32 v[30:33], v34, v148, v[30:33]
	v_mfma_f32_16x16x4_f32 v[2:5], v34, v149, v[2:5]
	v_mfma_f32_16x16x4_f32 v[30:33], v35, v150, v[30:33]
	v_mfma_f32_16x16x4_f32 v[2:5], v35, v151, v[2:5]
	v_mfma_f32_16x16x4_f32 v[30:33], v36, v152, v[30:33]
	v_mfma_f32_16x16x4_f32 v[2:5], v36, v153, v[2:5]
	v_mfma_f32_16x16x4_f32 v[30:33], v37, v154, v[30:33]
	v_mfma_f32_16x16x4_f32 v[2:5], v37, v155, v[2:5]
	ds_read_b128 v[34:37], v210 offset:768
	s_waitcnt lgkmcnt(0)
	v_mfma_f32_16x16x4_f32 v[30:33], v34, v156, v[30:33]
	v_mfma_f32_16x16x4_f32 v[2:5], v34, v157, v[2:5]
	v_mfma_f32_16x16x4_f32 v[30:33], v35, v158, v[30:33]
	v_mfma_f32_16x16x4_f32 v[2:5], v35, v159, v[2:5]
	v_mfma_f32_16x16x4_f32 v[30:33], v36, v160, v[30:33]
	v_mfma_f32_16x16x4_f32 v[2:5], v36, v161, v[2:5]
	v_mfma_f32_16x16x4_f32 v[30:33], v37, v162, v[30:33]
	v_mfma_f32_16x16x4_f32 v[2:5], v37, v163, v[2:5]
	ds_read_b128 v[34:37], v210 offset:832
	s_waitcnt lgkmcnt(0)
	v_mfma_f32_16x16x4_f32 v[30:33], v34, v164, v[30:33]
	v_mfma_f32_16x16x4_f32 v[2:5], v34, v165, v[2:5]
	v_mfma_f32_16x16x4_f32 v[30:33], v35, v166, v[30:33]
	v_mfma_f32_16x16x4_f32 v[2:5], v35, v167, v[2:5]
	v_mfma_f32_16x16x4_f32 v[30:33], v36, v168, v[30:33]
	v_mfma_f32_16x16x4_f32 v[2:5], v36, v169, v[2:5]
	v_mfma_f32_16x16x4_f32 v[30:33], v37, v170, v[30:33]
	v_mfma_f32_16x16x4_f32 v[2:5], v37, v171, v[2:5]
	ds_read_b128 v[34:37], v210 offset:896
	s_waitcnt lgkmcnt(0)
	v_mfma_f32_16x16x4_f32 v[30:33], v34, v172, v[30:33]
	v_mfma_f32_16x16x4_f32 v[2:5], v34, v173, v[2:5]
	v_mfma_f32_16x16x4_f32 v[30:33], v35, v174, v[30:33]
	v_mfma_f32_16x16x4_f32 v[2:5], v35, v175, v[2:5]
	v_mfma_f32_16x16x4_f32 v[30:33], v36, v176, v[30:33]
	v_mfma_f32_16x16x4_f32 v[2:5], v36, v177, v[2:5]
	v_mfma_f32_16x16x4_f32 v[30:33], v37, v178, v[30:33]
	v_mfma_f32_16x16x4_f32 v[2:5], v37, v179, v[2:5]
	ds_read_b128 v[34:37], v210 offset:960
	s_waitcnt lgkmcnt(0)
	v_mfma_f32_16x16x4_f32 v[30:33], v34, v180, v[30:33]
	v_mfma_f32_16x16x4_f32 v[2:5], v34, v181, v[2:5]
	v_mfma_f32_16x16x4_f32 v[30:33], v35, v182, v[30:33]
	v_mfma_f32_16x16x4_f32 v[2:5], v35, v183, v[2:5]
	v_mfma_f32_16x16x4_f32 v[30:33], v36, v184, v[30:33]
	v_mfma_f32_16x16x4_f32 v[2:5], v36, v185, v[2:5]
	v_mfma_f32_16x16x4_f32 v[30:33], v37, v186, v[30:33]
	v_mfma_f32_16x16x4_f32 v[2:5], v37, v187, v[2:5]
	s_nop 9
	ds_write2_b32 v211, v30, v2 offset1:16
	ds_write2_b32 v211, v31, v3 offset0:32 offset1:48
	ds_write2_b32 v211, v32, v4 offset0:64 offset1:80
	ds_write2_b32 v211, v33, v5 offset0:96 offset1:112
	s_waitcnt lgkmcnt(0)
	s_barrier
	global_load_dword v4, v[18:19], off
	ds_read2st64_b32 v[2:3], v198 offset1:8
	ds_bpermute_b32 v31, v192, v197
	s_waitcnt vmcnt(0) lgkmcnt(1)
	v_add_f32_e32 v2, v4, v2
	v_add_f32_e32 v4, v2, v3
	ds_read2st64_b32 v[2:3], v198 offset0:16 offset1:24
	s_waitcnt lgkmcnt(0)
	v_add_f32_e32 v2, v4, v2
	v_add_f32_e32 v4, v2, v3
	ds_read2st64_b32 v[2:3], v198 offset0:32 offset1:40
	s_waitcnt lgkmcnt(0)
	v_add_f32_e32 v2, v4, v2
	v_add_f32_e32 v4, v2, v3
	ds_read2st64_b32 v[2:3], v198 offset0:48 offset1:56
	s_waitcnt lgkmcnt(0)
	v_add_f32_e32 v2, v4, v2
	v_add_f32_e32 v3, v2, v3
	ds_bpermute_b32 v5, v192, v3
	s_waitcnt lgkmcnt(0)
	v_cmp_lt_f32_e64 s[20:21], v3, v5
	v_cmp_nlt_f32_e32 vcc, v3, v5
	s_and_saveexec_b64 s[22:23], vcc
	v_cmp_eq_f32_e32 vcc, v3, v5
	v_cmp_lt_i32_e64 s[0:1], v31, v197
	s_and_b64 s[0:1], vcc, s[0:1]
	s_andn2_b64 s[20:21], s[20:21], exec
	s_and_b64 s[0:1], s[0:1], exec
	s_or_b64 s[20:21], s[20:21], s[0:1]
	s_or_b64 exec, exec, s[22:23]
	v_mov_b32_e32 v4, v3
	v_mov_b32_e32 v30, v3
	v_mov_b32_e32 v2, v197
	s_and_saveexec_b64 s[0:1], s[20:21]
	v_mov_b32_e32 v4, v5
	v_mov_b32_e32 v30, v5
	v_mov_b32_e32 v2, v31
	s_or_b64 exec, exec, s[0:1]
	ds_bpermute_b32 v5, v193, v4
	ds_bpermute_b32 v31, v193, v2
	s_waitcnt lgkmcnt(1)
	v_cmp_lt_f32_e64 s[20:21], v30, v5
	v_cmp_nlt_f32_e32 vcc, v30, v5
	s_and_saveexec_b64 s[22:23], vcc
	s_cbranch_execz .LBB0_688
	v_cmp_eq_f32_e32 vcc, v30, v5
	s_waitcnt lgkmcnt(0)
	v_cmp_lt_i32_e64 s[0:1], v31, v2
	s_and_b64 s[0:1], vcc, s[0:1]
	s_andn2_b64 s[20:21], s[20:21], exec
	s_and_b64 s[0:1], s[0:1], exec
	s_or_b64 s[20:21], s[20:21], s[0:1]
